# c21
# speedup vs baseline: 1.0007x; 1.0007x over previous
.LBB2_6:
	s_mov_b32 s6, 0
	s_ashr_i32 s7, s6, 31
	v_add_u32_e32 v144, s6, v0
	v_ashrrev_i32_e32 v0, 7, v144
	v_and_b32_e32 v0, -2, v0
	v_bfe_u32 v147, v144, 5, 1
	v_lshl_add_u32 v148, s14, 2, v0
	v_bfe_u32 v146, v144, 4, 1
	s_lshl_b64 s[4:5], s[6:7], 2
	s_add_u32 s0, s8, s4
	s_addc_u32 s1, s9, s5
	s_add_u32 s4, s10, s4
	s_addc_u32 s5, s11, s5
	v_ashrrev_i32_e32 v0, 1, v148
	v_lshl_add_u32 v0, s2, 6, v0
	s_movk_i32 s3, 0x6000
	v_mov_b64_e32 v[46:47], s[12:13]
	v_ashrrev_i32_e32 v1, 31, v0
	v_mad_i64_i32 v[148:149], s[2:3], v0, s3, v[46:47]
	v_lshlrev_b64 v[0:1], 10, v[0:1]
	s_mov_b64 s[6:7], 0x3000000
	v_permlane32_swap_b32_e32 v30, v14
	v_permlane32_swap_b32_e32 v31, v15
	v_lshl_add_u64 v[0:1], s[12:13], 0, v[0:1]
	v_permlane32_swap_b32_e32 v32, v16
	v_permlane32_swap_b32_e32 v33, v17
	s_mov_b32 s4, 0xbfb8aa3b
	v_and_b32_e32 v163, 0xcf, v144
	v_lshlrev_b32_e32 v162, 9, v147
	v_mul_u32_u24_e32 v144, 12, v146
	v_cmp_eq_u32_e64 s[0:1], 0, v146
	v_lshl_add_u64 v[146:147], v[0:1], 0, s[6:7]
	v_permlane32_swap_b32_e32 v26, v10
	v_permlane32_swap_b32_e32 v27, v11
	v_permlane32_swap_b32_e32 v22, v6
	v_permlane32_swap_b32_e32 v23, v7
	v_permlane32_swap_b32_e32 v28, v12
	v_permlane32_swap_b32_e32 v29, v13
	v_permlane32_swap_b32_e32 v24, v8
	v_permlane32_swap_b32_e32 v25, v9
	v_permlane32_swap_b32_e32 v18, v2
	v_permlane32_swap_b32_e32 v19, v3
	v_permlane32_swap_b32_e32 v20, v4
	v_permlane32_swap_b32_e32 v21, v5
	s_mov_b32 s3, 0x700000
	s_mov_b32 s8, 0x42000000
	s_mov_b32 s2, 0xc2000000
	v_mov_b32_e32 v145, 0
	s_waitcnt vmcnt(0)
	v_pk_mul_f32 v[0:1], v[184:185], v[30:31]
	v_pk_mul_f32 v[30:31], v[186:187], v[32:33]
	v_pk_mul_f32 v[32:33], v[0:1], s[4:5] op_sel_hi:[1,0]
	v_pk_mul_f32 v[34:35], v[30:31], s[4:5] op_sel_hi:[1,0]
	v_exp_f32_e32 v32, v32
	v_exp_f32_e32 v33, v33
	v_exp_f32_e32 v34, v34
	v_exp_f32_e32 v35, v35
	v_pk_mul_f32 v[26:27], v[188:189], v[26:27]
	v_pk_add_f32 v[32:33], v[32:33], 1.0 op_sel_hi:[1,0]
	v_pk_mul_f32 v[22:23], v[192:193], v[22:23]
	v_rcp_f32_e32 v32, v32
	v_rcp_f32_e32 v33, v33
	v_pk_add_f32 v[34:35], v[34:35], 1.0 op_sel_hi:[1,0]
	v_pk_mul_f32 v[24:25], v[194:195], v[24:25]
	v_rcp_f32_e32 v34, v34
	v_rcp_f32_e32 v35, v35
	v_pk_mul_f32 v[0:1], v[0:1], v[32:33]
	v_pk_mul_f32 v[18:19], v[196:197], v[18:19]
	v_pk_mul_f32 v[0:1], v[26:27], v[0:1]
	v_pk_mul_f32 v[26:27], v[190:191], v[28:29]
	v_pk_mul_f32 v[28:29], v[30:31], v[34:35]
	v_pk_mul_f32 v[30:31], v[24:25], s[4:5] op_sel_hi:[1,0]
	v_pk_mul_f32 v[26:27], v[26:27], v[28:29]
	v_pk_mul_f32 v[28:29], v[22:23], s[4:5] op_sel_hi:[1,0]
	v_exp_f32_e32 v30, v30
	v_exp_f32_e32 v28, v28
	v_exp_f32_e32 v29, v29
	v_exp_f32_e32 v31, v31
	v_pk_mul_f32 v[20:21], v[198:199], v[20:21]
	v_pk_mul_f32 v[14:15], v[200:201], v[14:15]
	v_pk_add_f32 v[28:29], v[28:29], 1.0 op_sel_hi:[1,0]
	v_pk_add_f32 v[30:31], v[30:31], 1.0 op_sel_hi:[1,0]
	v_rcp_f32_e32 v28, v28
	v_rcp_f32_e32 v29, v29
	v_rcp_f32_e32 v30, v30
	v_rcp_f32_e32 v31, v31
	v_pk_mul_f32 v[16:17], v[202:203], v[16:17]
	v_pk_mul_f32 v[22:23], v[22:23], v[28:29]
	v_pk_mul_f32 v[10:11], v[204:205], v[10:11]
	v_pk_mul_f32 v[18:19], v[18:19], v[22:23]
	v_pk_mul_f32 v[22:23], v[24:25], v[30:31]
	v_pk_mul_f32 v[24:25], v[16:17], s[4:5] op_sel_hi:[1,0]
	v_pk_mul_f32 v[20:21], v[20:21], v[22:23]
	v_pk_mul_f32 v[22:23], v[14:15], s[4:5] op_sel_hi:[1,0]
	v_exp_f32_e32 v24, v24
	v_exp_f32_e32 v22, v22
	v_exp_f32_e32 v23, v23
	v_exp_f32_e32 v25, v25
	v_pk_mul_f32 v[12:13], v[206:207], v[12:13]
	v_pk_mul_f32 v[6:7], v[208:209], v[6:7]
	v_pk_add_f32 v[22:23], v[22:23], 1.0 op_sel_hi:[1,0]
	v_pk_add_f32 v[24:25], v[24:25], 1.0 op_sel_hi:[1,0]
	v_rcp_f32_e32 v22, v22
	v_rcp_f32_e32 v23, v23
	v_rcp_f32_e32 v24, v24
	v_rcp_f32_e32 v25, v25
	v_pk_mul_f32 v[8:9], v[210:211], v[8:9]
	v_pk_mul_f32 v[14:15], v[14:15], v[22:23]
	v_pk_mul_f32 v[2:3], v[212:213], v[2:3]
	v_pk_mul_f32 v[10:11], v[10:11], v[14:15]
	v_pk_mul_f32 v[14:15], v[16:17], v[24:25]
	v_pk_mul_f32 v[16:17], v[8:9], s[4:5] op_sel_hi:[1,0]
	v_pk_mul_f32 v[12:13], v[12:13], v[14:15]
	v_pk_mul_f32 v[14:15], v[6:7], s[4:5] op_sel_hi:[1,0]
	v_exp_f32_e32 v16, v16
	v_exp_f32_e32 v14, v14
	v_exp_f32_e32 v15, v15
	v_exp_f32_e32 v17, v17
	v_pk_mul_f32 v[4:5], v[214:215], v[4:5]
	v_mov_b32_e32 v164, 0xffffff7f
	v_pk_add_f32 v[14:15], v[14:15], 1.0 op_sel_hi:[1,0]
	v_pk_add_f32 v[16:17], v[16:17], 1.0 op_sel_hi:[1,0]
	v_rcp_f32_e32 v14, v14
	v_rcp_f32_e32 v15, v15
	v_rcp_f32_e32 v16, v16
	v_rcp_f32_e32 v17, v17
	s_movk_i32 s5, 0xff9c
	v_pk_mul_f32 v[6:7], v[6:7], v[14:15]
	v_mov_b32_e32 v165, 0x64
	v_pk_mul_f32 v[2:3], v[2:3], v[6:7]
	v_pk_mul_f32 v[6:7], v[8:9], v[16:17]
	v_pk_mul_f32 v[4:5], v[4:5], v[6:7]
	v_max3_f32 v6, |v20|, |v21|, |v0|
	v_max3_f32 v6, v6, |v1|, |v26|
	v_max3_f32 v6, v6, |v27|, |v18|
	v_max3_f32 v6, v6, |v19|, |v10|
	v_max3_f32 v6, v6, |v11|, |v12|
	v_max3_f32 v6, v6, |v13|, |v2|
	v_max3_f32 v6, v6, |v3|, |v4|
	v_max_f32_e64 v6, v6, |v5|
	v_mov_b32_e32 v7, v6
	s_nop 1
	v_permlane16_swap_b32_e32 v6, v7
	v_max_f32_e32 v6, v6, v7
	v_lshrrev_b32_e32 v7, 23, v6
	v_and_b32_e32 v6, 0x7fffff, v6
	v_cmp_lt_u32_e32 vcc, s3, v6
	s_nop 1
	v_addc_co_u32_e32 v6, vcc, v7, v164, vcc
	v_med3_i32 v166, v6, s5, v165
	v_lshlrev_b32_e32 v6, 23, v166
	v_sub_u32_e32 v6, 1.0, v6
	v_pk_mul_f32 v[40:41], v[6:7], v[10:11] op_sel_hi:[0,1]
	v_pk_mul_f32 v[42:43], v[6:7], v[12:13] op_sel_hi:[0,1]
	v_pk_mul_f32 v[44:45], v[6:7], v[2:3] op_sel_hi:[0,1]
	v_pk_mul_f32 v[46:47], v[6:7], v[4:5] op_sel_hi:[0,1]
	v_pk_mul_f32 v[32:33], v[6:7], v[0:1] op_sel_hi:[0,1]
	v_pk_mul_f32 v[34:35], v[6:7], v[26:27] op_sel_hi:[0,1]
	v_pk_mul_f32 v[36:37], v[6:7], v[18:19] op_sel_hi:[0,1]
	v_pk_mul_f32 v[38:39], v[6:7], v[20:21] op_sel_hi:[0,1]
	v_cvt_scalef32_2xpk16_fp6_f32 v[168:173], v[32:47], v[40:55], 1.0
	v_cvt_scalef32_pk32_f32_fp6 v[0:31], v[168:173], s8
	v_fma_f32 v16, v32, s2, v0
	v_fma_f32 v17, v33, s2, v2
	v_fma_f32 v18, v34, s2, v4
	v_fma_f32 v19, v35, s2, v6
	v_fma_f32 v20, v36, s2, v8
	v_fma_f32 v21, v37, s2, v10
	v_fma_f32 v22, v38, s2, v12
	v_fma_f32 v23, v39, s2, v14
	v_fma_f32 v24, v40, s2, v1
	v_fma_f32 v25, v41, s2, v3
	v_fma_f32 v26, v42, s2, v5
	v_fma_f32 v27, v43, s2, v7
	v_fma_f32 v28, v44, s2, v9
	v_fma_f32 v29, v45, s2, v11
	v_fma_f32 v30, v46, s2, v13
	v_fma_f32 v31, v47, s2, v15
	v_cvt_scalef32_2xpk16_fp6_f32 v[0:5], v[16:31], v[24:39], 1.0
	v_or_b32_e32 v3, v163, v162
	v_mul_u32_u24_e32 v4, 24, v3
	v_mov_b32_e32 v5, v145
	v_lshl_add_u64 v[4:5], v[148:149], 0, v[4:5]
	v_lshl_add_u64 v[4:5], v[4:5], 0, v[144:145]
	global_store_dwordx3 v[4:5], v[168:170], off nt
	v_add_co_u32_e32 v4, vcc, 0x1000, v4
	v_xor_b32_e32 v0, 0x20820820, v0
	v_xor_b32_e32 v1, 0x8208208, v1
	v_xor_b32_e32 v2, 0x82082082, v2
	v_addc_co_u32_e32 v5, vcc, 0, v5, vcc
	global_store_dwordx3 v[4:5], v[0:2], off offset:2048 nt
	s_and_saveexec_b64 s[6:7], s[0:1]
	s_cbranch_execz .LBB2_8
	v_mov_b32_e32 v1, 0x7a00
	v_add_u32_e32 v0, 0x7f, v166
	v_lshl_add_u32 v1, v166, 8, v1
	v_or_b32_e32 v2, v1, v0
	v_lshl_or_b32 v0, v163, 1, v162
	v_mov_b32_e32 v1, v145
	v_lshl_add_u64 v[0:1], v[146:147], 0, v[0:1]
	global_store_short v[0:1], v2, off

.LBB3_6:
	s_mov_b32 s0, 0
	s_ashr_i32 s1, s0, 31
	v_add_u32_e32 v26, s0, v0
	v_ashrrev_i32_e32 v0, 6, v26
	v_and_b32_e32 v0, -4, v0
	v_bfe_u32 v177, v26, 5, 1
	v_lshl_add_u32 v178, s12, 3, v0
	v_bfe_u32 v27, v26, 4, 1
	v_or_b32_e32 v0, v178, v177
	s_lshl_b64 s[4:5], s[0:1], 2
	v_lshlrev_b32_e32 v36, 5, v0
	v_lshlrev_b32_e32 v179, 2, v27
	s_add_u32 s4, s10, s4
	s_addc_u32 s5, s11, s5
	v_ashrrev_i32_e32 v31, 31, v36
	v_and_b32_e32 v181, 0xcf, v26
	v_mul_u32_u24_e32 v160, 12, v27
	v_cmp_eq_u32_e64 s[0:1], 0, v27
	s_lshl_b32 s11, s8, 6
	v_ashrrev_i32_e32 v30, 1, v178
	v_or_b32_e32 v176, 8, v179
	v_add_u32_e32 v34, s11, v30
	s_movk_i32 s9, 0x6000
	v_mov_b64_e32 v[32:33], s[2:3]
	s_add_u32 s6, s2, 0x3000000
	v_ashrrev_i32_e32 v35, 31, v34
	v_or_b32_e32 v30, v36, v176
	s_addc_u32 s7, s3, 0
	v_mad_i64_i32 v[168:169], s[8:9], v34, s9, v[32:33]
	v_lshlrev_b64 v[32:33], 10, v[34:35]
	v_lshl_add_u64 v[166:167], s[6:7], 0, v[32:33]
	v_permlane32_swap_b32_e32 v14, v6
	v_permlane32_swap_b32_e32 v15, v7
	v_permlane32_swap_b32_e32 v16, v8
	v_permlane32_swap_b32_e32 v17, v9
	v_permlane32_swap_b32_e32 v10, v2
	v_permlane32_swap_b32_e32 v11, v3
	s_mov_b32 s20, 0x3e6d3388
	s_mov_b32 s22, 0xbf3a00e3
	s_mov_b32 s16, 0x3f07dc22
	s_mov_b32 s14, 0xbf38aa3b
	v_mov_b64_e32 v[0:1], s[22:23]
	s_mov_b32 s18, 0x3f35f0e3
	s_mov_b32 s10, 0xbe11a98e
	s_mov_b32 s12, 0x3e027906
	v_permlane32_swap_b32_e32 v12, v4
	v_permlane32_swap_b32_e32 v13, v5
	s_mov_b32 s9, 0x700000
	v_mov_b32_e32 v182, 0xffffff7f
	v_mov_b32_e32 v183, 0x64
	s_mov_b32 s8, 0xc2000000
	v_lshlrev_b32_e32 v180, 9, v177
	v_mov_b32_e32 v161, 0
	v_mov_b32_e32 v165, v161
	v_lshl_or_b32 v162, v181, 1, v180
	s_waitcnt vmcnt(4)
	v_pk_mul_f32 v[14:15], v[192:193], v[14:15]
	s_nop 0
	v_and_b32_e32 v19, 0x7fffffff, v15
	v_and_b32_e32 v18, 0x7fffffff, v14
	v_pk_mul_f32 v[16:17], v[194:195], v[16:17]
	v_pk_mul_f32 v[10:11], v[196:197], v[10:11]
	v_pk_fma_f32 v[22:23], v[18:19], s[20:21], 1.0 op_sel_hi:[1,0,0]
	v_and_b32_e32 v35, 0x7fffffff, v17
	v_and_b32_e32 v34, 0x7fffffff, v16
	v_rcp_f32_e32 v22, v22
	v_rcp_f32_e32 v23, v23
	v_pk_fma_f32 v[38:39], v[34:35], s[20:21], 1.0 op_sel_hi:[1,0,0]
	v_pk_mul_f32 v[20:21], v[14:15], v[14:15]
	v_rcp_f32_e32 v38, v38
	v_rcp_f32_e32 v39, v39
	v_pk_mul_f32 v[20:21], v[20:21], s[14:15] op_sel_hi:[1,0]
	v_pk_fma_f32 v[44:45], v[22:23], s[16:17], v[0:1] op_sel_hi:[1,0,0]
	v_pk_mul_f32 v[36:37], v[16:17], v[16:17]
	v_exp_f32_e32 v20, v20
	v_exp_f32_e32 v21, v21
	v_pk_fma_f32 v[44:45], v[22:23], v[44:45], s[18:19] op_sel_hi:[1,1,0]
	v_pk_mul_f32 v[36:37], v[36:37], s[14:15] op_sel_hi:[1,0]
	v_pk_fma_f32 v[46:47], v[38:39], s[16:17], v[0:1] op_sel_hi:[1,0,0]
	v_pk_fma_f32 v[44:45], v[22:23], v[44:45], s[10:11] op_sel_hi:[1,1,0]
	v_and_b32_e32 v41, 0x7fffffff, v11
	v_and_b32_e32 v40, 0x7fffffff, v10
	v_exp_f32_e32 v36, v36
	v_exp_f32_e32 v37, v37
	v_pk_fma_f32 v[46:47], v[38:39], v[46:47], s[18:19] op_sel_hi:[1,1,0]
	v_pk_fma_f32 v[44:45], v[22:23], v[44:45], s[12:13] op_sel_hi:[1,1,0]
	v_pk_fma_f32 v[42:43], v[40:41], s[20:21], 1.0 op_sel_hi:[1,0,0]
	v_pk_fma_f32 v[46:47], v[38:39], v[46:47], s[10:11] op_sel_hi:[1,1,0]
	v_pk_mul_f32 v[22:23], v[22:23], v[44:45]
	v_rcp_f32_e32 v42, v42
	v_pk_fma_f32 v[46:47], v[38:39], v[46:47], s[12:13] op_sel_hi:[1,1,0]
	v_pk_fma_f32 v[20:21], v[20:21], v[22:23], 0.5 op_sel_hi:[1,1,0] neg_lo:[1,0,0] neg_hi:[1,0,0]
	v_rcp_f32_e32 v43, v43
	v_pk_mul_f32 v[38:39], v[38:39], v[46:47]
	v_pk_mul_f32 v[18:19], v[18:19], v[20:21]
	v_pk_mul_f32 v[20:21], v[10:11], v[10:11]
	v_pk_fma_f32 v[14:15], v[14:15], 0.5, v[18:19] op_sel_hi:[1,0,1]
	v_pk_fma_f32 v[18:19], v[36:37], v[38:39], 0.5 op_sel_hi:[1,1,0] neg_lo:[1,0,0] neg_hi:[1,0,0]
	v_pk_mul_f32 v[20:21], v[20:21], s[14:15] op_sel_hi:[1,0]
	v_pk_mul_f32 v[18:19], v[34:35], v[18:19]
	v_pk_mul_f32 v[12:13], v[198:199], v[12:13]
	v_pk_fma_f32 v[16:17], v[16:17], 0.5, v[18:19] op_sel_hi:[1,0,1]
	v_pk_fma_f32 v[18:19], v[42:43], s[16:17], v[0:1] op_sel_hi:[1,0,0]
	v_exp_f32_e32 v20, v20
	v_pk_fma_f32 v[18:19], v[42:43], v[18:19], s[18:19] op_sel_hi:[1,1,0]
	v_exp_f32_e32 v21, v21
	v_and_b32_e32 v23, 0x7fffffff, v13
	v_and_b32_e32 v22, 0x7fffffff, v12
	v_pk_fma_f32 v[18:19], v[42:43], v[18:19], s[10:11] op_sel_hi:[1,1,0]
	v_pk_fma_f32 v[24:25], v[22:23], s[20:21], 1.0 op_sel_hi:[1,0,0]
	v_pk_fma_f32 v[18:19], v[42:43], v[18:19], s[12:13] op_sel_hi:[1,1,0]
	v_rcp_f32_e32 v24, v24
	v_rcp_f32_e32 v25, v25
	v_pk_mul_f32 v[18:19], v[42:43], v[18:19]
	v_pk_mul_f32 v[6:7], v[200:201], v[6:7]
	v_pk_fma_f32 v[18:19], v[20:21], v[18:19], 0.5 op_sel_hi:[1,1,0] neg_lo:[1,0,0] neg_hi:[1,0,0]
	v_pk_mul_f32 v[20:21], v[12:13], v[12:13]
	v_pk_mul_f32 v[18:19], v[40:41], v[18:19]
	v_pk_mul_f32 v[20:21], v[20:21], s[14:15] op_sel_hi:[1,0]
	v_pk_fma_f32 v[10:11], v[10:11], 0.5, v[18:19] op_sel_hi:[1,0,1]
	v_pk_fma_f32 v[18:19], v[24:25], s[16:17], v[0:1] op_sel_hi:[1,0,0]
	v_exp_f32_e32 v20, v20
	v_pk_fma_f32 v[18:19], v[24:25], v[18:19], s[18:19] op_sel_hi:[1,1,0]
	v_exp_f32_e32 v21, v21
	v_pk_fma_f32 v[18:19], v[24:25], v[18:19], s[10:11] op_sel_hi:[1,1,0]
	v_pk_mul_f32 v[8:9], v[202:203], v[8:9]
	v_pk_fma_f32 v[18:19], v[24:25], v[18:19], s[12:13] op_sel_hi:[1,1,0]
	v_pk_mul_f32 v[2:3], v[204:205], v[2:3]
	v_pk_mul_f32 v[18:19], v[24:25], v[18:19]
	v_and_b32_e32 v25, 0x7fffffff, v7
	v_and_b32_e32 v24, 0x7fffffff, v6
	v_pk_fma_f32 v[26:27], v[24:25], s[20:21], 1.0 op_sel_hi:[1,0,0]
	v_pk_fma_f32 v[18:19], v[20:21], v[18:19], 0.5 op_sel_hi:[1,1,0] neg_lo:[1,0,0] neg_hi:[1,0,0]
	v_rcp_f32_e32 v26, v26
	v_rcp_f32_e32 v27, v27
	v_pk_mul_f32 v[18:19], v[22:23], v[18:19]
	v_pk_mul_f32 v[20:21], v[6:7], v[6:7]
	v_pk_fma_f32 v[12:13], v[12:13], 0.5, v[18:19] op_sel_hi:[1,0,1]
	v_pk_fma_f32 v[18:19], v[26:27], s[16:17], v[0:1] op_sel_hi:[1,0,0]
	v_pk_mul_f32 v[20:21], v[20:21], s[14:15] op_sel_hi:[1,0]
	v_pk_fma_f32 v[18:19], v[26:27], v[18:19], s[18:19] op_sel_hi:[1,1,0]
	v_exp_f32_e32 v20, v20
	v_pk_fma_f32 v[18:19], v[26:27], v[18:19], s[10:11] op_sel_hi:[1,1,0]
	v_exp_f32_e32 v21, v21
	v_pk_fma_f32 v[18:19], v[26:27], v[18:19], s[12:13] op_sel_hi:[1,1,0]
	v_and_b32_e32 v23, 0x7fffffff, v9
	v_and_b32_e32 v22, 0x7fffffff, v8
	v_pk_mul_f32 v[18:19], v[26:27], v[18:19]
	v_pk_fma_f32 v[26:27], v[22:23], s[20:21], 1.0 op_sel_hi:[1,0,0]
	v_pk_fma_f32 v[18:19], v[20:21], v[18:19], 0.5 op_sel_hi:[1,1,0] neg_lo:[1,0,0] neg_hi:[1,0,0]
	v_rcp_f32_e32 v26, v26
	v_rcp_f32_e32 v27, v27
	v_pk_mul_f32 v[18:19], v[24:25], v[18:19]
	v_pk_mul_f32 v[20:21], v[8:9], v[8:9]
	v_pk_fma_f32 v[6:7], v[6:7], 0.5, v[18:19] op_sel_hi:[1,0,1]
	v_pk_fma_f32 v[18:19], v[26:27], s[16:17], v[0:1] op_sel_hi:[1,0,0]
	v_pk_mul_f32 v[20:21], v[20:21], s[14:15] op_sel_hi:[1,0]
	v_pk_fma_f32 v[18:19], v[26:27], v[18:19], s[18:19] op_sel_hi:[1,1,0]
	v_exp_f32_e32 v20, v20
	v_pk_fma_f32 v[18:19], v[26:27], v[18:19], s[10:11] op_sel_hi:[1,1,0]
	v_exp_f32_e32 v21, v21
	v_pk_fma_f32 v[18:19], v[26:27], v[18:19], s[12:13] op_sel_hi:[1,1,0]
	v_and_b32_e32 v25, 0x7fffffff, v3
	v_and_b32_e32 v24, 0x7fffffff, v2
	v_pk_mul_f32 v[18:19], v[26:27], v[18:19]
	v_pk_fma_f32 v[26:27], v[24:25], s[20:21], 1.0 op_sel_hi:[1,0,0]
	v_pk_fma_f32 v[18:19], v[20:21], v[18:19], 0.5 op_sel_hi:[1,1,0] neg_lo:[1,0,0] neg_hi:[1,0,0]
	v_rcp_f32_e32 v26, v26
	v_rcp_f32_e32 v27, v27
	v_pk_mul_f32 v[18:19], v[22:23], v[18:19]
	v_pk_mul_f32 v[20:21], v[2:3], v[2:3]
	v_pk_fma_f32 v[8:9], v[8:9], 0.5, v[18:19] op_sel_hi:[1,0,1]
	v_pk_fma_f32 v[18:19], v[26:27], s[16:17], v[0:1] op_sel_hi:[1,0,0]
	v_pk_mul_f32 v[20:21], v[20:21], s[14:15] op_sel_hi:[1,0]
	v_pk_fma_f32 v[18:19], v[26:27], v[18:19], s[18:19] op_sel_hi:[1,1,0]
	v_exp_f32_e32 v20, v20
	v_pk_fma_f32 v[18:19], v[26:27], v[18:19], s[10:11] op_sel_hi:[1,1,0]
	v_exp_f32_e32 v21, v21
	v_pk_mul_f32 v[4:5], v[206:207], v[4:5]
	v_pk_fma_f32 v[18:19], v[26:27], v[18:19], s[12:13] op_sel_hi:[1,1,0]
	v_and_b32_e32 v23, 0x7fffffff, v5
	v_and_b32_e32 v22, 0x7fffffff, v4
	v_pk_mul_f32 v[18:19], v[26:27], v[18:19]
	v_pk_fma_f32 v[26:27], v[22:23], s[20:21], 1.0 op_sel_hi:[1,0,0]
	v_pk_fma_f32 v[18:19], v[20:21], v[18:19], 0.5 op_sel_hi:[1,1,0] neg_lo:[1,0,0] neg_hi:[1,0,0]
	v_rcp_f32_e32 v26, v26
	v_rcp_f32_e32 v27, v27
	v_pk_mul_f32 v[18:19], v[24:25], v[18:19]
	v_pk_fma_f32 v[0:1], v[26:27], s[16:17], v[0:1] op_sel_hi:[1,0,0]
	v_pk_fma_f32 v[2:3], v[2:3], 0.5, v[18:19] op_sel_hi:[1,0,1]
	v_pk_mul_f32 v[18:19], v[4:5], v[4:5]
	v_pk_fma_f32 v[0:1], v[26:27], v[0:1], s[18:19] op_sel_hi:[1,1,0]
	v_pk_mul_f32 v[18:19], v[18:19], s[14:15] op_sel_hi:[1,0]
	v_pk_fma_f32 v[0:1], v[26:27], v[0:1], s[10:11] op_sel_hi:[1,1,0]
	v_exp_f32_e32 v18, v18
	v_exp_f32_e32 v19, v19
	v_pk_fma_f32 v[0:1], v[26:27], v[0:1], s[12:13] op_sel_hi:[1,1,0]
	s_movk_i32 s13, 0xff9c
	v_pk_mul_f32 v[0:1], v[26:27], v[0:1]
	s_mov_b32 s15, 0x42000000
	v_pk_fma_f32 v[0:1], v[18:19], v[0:1], 0.5 op_sel_hi:[1,1,0] neg_lo:[1,0,0] neg_hi:[1,0,0]
	v_pk_mul_f32 v[0:1], v[22:23], v[0:1]
	s_nop 0
	v_pk_fma_f32 v[0:1], v[4:5], 0.5, v[0:1] op_sel_hi:[1,0,1]
	v_max3_f32 v4, |v12|, |v13|, |v14|
	v_max3_f32 v4, v4, |v15|, |v16|
	v_max3_f32 v4, v4, |v17|, |v10|
	v_max3_f32 v4, v4, |v11|, |v6|
	v_max3_f32 v4, v4, |v7|, |v8|
	v_max3_f32 v4, v4, |v9|, |v2|
	v_max3_f32 v4, v4, |v3|, |v0|
	v_max_f32_e64 v4, v4, |v1|
	v_mov_b32_e32 v5, v4
	s_nop 1
	v_permlane16_swap_b32_e32 v4, v5
	v_max_f32_e32 v4, v4, v5
	v_lshrrev_b32_e32 v5, 23, v4
	v_and_b32_e32 v4, 0x7fffff, v4
	v_cmp_lt_u32_e32 vcc, s9, v4
	s_nop 1
	v_addc_co_u32_e32 v4, vcc, v5, v182, vcc
	v_med3_i32 v163, v4, s13, v183
	v_lshlrev_b32_e32 v4, 23, v163
	v_sub_u32_e32 v4, 1.0, v4
	v_pk_mul_f32 v[40:41], v[4:5], v[6:7] op_sel_hi:[0,1]
	v_pk_mul_f32 v[42:43], v[4:5], v[8:9] op_sel_hi:[0,1]
	v_pk_mul_f32 v[44:45], v[4:5], v[2:3] op_sel_hi:[0,1]
	v_pk_mul_f32 v[46:47], v[4:5], v[0:1] op_sel_hi:[0,1]
	v_pk_mul_f32 v[32:33], v[4:5], v[14:15] op_sel_hi:[0,1]
	v_pk_mul_f32 v[34:35], v[4:5], v[16:17] op_sel_hi:[0,1]
	v_pk_mul_f32 v[36:37], v[4:5], v[10:11] op_sel_hi:[0,1]
	v_pk_mul_f32 v[38:39], v[4:5], v[12:13] op_sel_hi:[0,1]
	v_cvt_scalef32_2xpk16_fp6_f32 v[184:189], v[32:47], v[40:55], 1.0
	v_cvt_scalef32_pk32_f32_fp6 v[0:31], v[184:189], s15
	v_fma_f32 v16, v32, s8, v0
	v_fma_f32 v17, v33, s8, v2
	v_fma_f32 v18, v34, s8, v4
	v_fma_f32 v19, v35, s8, v6
	v_fma_f32 v20, v36, s8, v8
	v_fma_f32 v21, v37, s8, v10
	v_fma_f32 v22, v38, s8, v12
	v_fma_f32 v23, v39, s8, v14
	v_fma_f32 v24, v40, s8, v1
	v_fma_f32 v25, v41, s8, v3
	v_fma_f32 v26, v42, s8, v5
	v_fma_f32 v27, v43, s8, v7
	v_fma_f32 v28, v44, s8, v9
	v_fma_f32 v29, v45, s8, v11
	v_fma_f32 v30, v46, s8, v13
	v_fma_f32 v31, v47, s8, v15
	v_cvt_scalef32_2xpk16_fp6_f32 v[0:5], v[16:31], v[24:39], 1.0
	v_or_b32_e32 v3, v181, v180
	v_mul_u32_u24_e32 v164, 24, v3
	v_lshl_add_u64 v[4:5], v[168:169], 0, v[164:165]
	v_lshl_add_u64 v[4:5], v[4:5], 0, v[160:161]
	global_store_dwordx3 v[4:5], v[184:186], off nt
	v_add_co_u32_e32 v4, vcc, 0x1000, v4
	v_xor_b32_e32 v0, 0x20820820, v0
	v_xor_b32_e32 v1, 0x8208208, v1
	v_xor_b32_e32 v2, 0x82082082, v2
	v_addc_co_u32_e32 v5, vcc, 0, v5, vcc
	global_store_dwordx3 v[4:5], v[0:2], off offset:2048 nt
	s_and_saveexec_b64 s[24:25], s[0:1]
	s_cbranch_execz .LBB3_8
	v_mov_b32_e32 v1, 0x7a00
	v_add_u32_e32 v0, 0x7f, v163
	v_lshl_add_u32 v1, v163, 8, v1
	v_mov_b32_e32 v163, v161
	v_or_b32_e32 v2, v1, v0
	v_lshl_add_u64 v[0:1], v[166:167], 0, v[162:163]
	global_store_short v[0:1], v2, off
